# speedup vs baseline: 1.0923x; 1.0140x over previous
_Z11knrm_kernelPKfS0_PKiS2_S0_Pf:
	s_load_dwordx8 s[4:11], s[0:1], 0x0
	s_load_dwordx4 s[12:15], s[0:1], 0x20
	v_lshrrev_b32_e32 v1, 6, v0
	v_and_b32_e32 v120, 63, v0
	v_lshrrev_b32_e32 v100, 4, v0
	v_and_b32_e32 v123, 15, v0
	v_lshlrev_b32_e32 v124, 5, v1
	s_lshl_b32 s3, s2, 5
	v_lshl_or_b32 v8, s2, 8, v124
	v_or_b32_e32 v2, s3, v100
	s_movk_i32 s3, 0x4b0
	v_mul_lo_u32 v2, v2, s3
	v_mul_lo_u32 v99, v8, s3
	v_lshlrev_b32_e32 v132, 4, v120
	v_min_u32_e32 v193, 23, v120
	v_lshl_add_u32 v3, v123, 4, v2
	v_min_u32_e32 v4, 10, v123
	v_add_u32_e32 v192, v99, v132
	v_lshlrev_b32_e32 v193, 4, v193
	s_movk_i32 s27, 0x1000
	s_movk_i32 s28, 0x2000
	v_lshl_add_u32 v2, v4, 4, v2
	v_add3_u32 v193, v99, v193, s28
	s_mov_b32 s19, 0x20000
	s_mov_b32 s18, 0x4b00000
	s_waitcnt lgkmcnt(0)
	s_mov_b64 s[16:17], s[6:7]
	s_and_b32 s5, s5, 0xffff
	s_mov_b32 s6, 0x960000
	s_mov_b32 s7, s19
	s_and_b32 s17, s17, 0xffff
	buffer_load_dwordx4 v[90:93], v3, s[4:7], 0 offen nt
	buffer_load_dwordx4 v[86:89], v3, s[4:7], 0 offen offset:256 nt
	buffer_load_dwordx4 v[82:85], v3, s[4:7], 0 offen offset:512 nt
	buffer_load_dwordx4 v[78:81], v3, s[4:7], 0 offen offset:768 nt
	buffer_load_dwordx4 v[94:97], v2, s[4:7], 0 offen offset:1024 nt
	buffer_load_dwordx4 v[2:5], v192, s[16:19], 0 offen nt
	buffer_load_dwordx4 v[14:17], v192, s[16:19], 0 offen offset:1024 nt
	buffer_load_dwordx4 v[34:37], v192, s[16:19], 0 offen offset:2048 nt
	buffer_load_dwordx4 v[46:49], v192, s[16:19], 0 offen offset:3072 nt
	buffer_load_dwordx4 v[54:57], v192, s[16:19], s27 offen nt
	buffer_load_dwordx4 v[58:61], v192, s[16:19], s27 offen offset:1024 nt
	buffer_load_dwordx4 v[62:65], v192, s[16:19], s27 offen offset:2048 nt
	buffer_load_dwordx4 v[66:69], v192, s[16:19], s27 offen offset:3072 nt
	buffer_load_dwordx4 v[70:73], v192, s[16:19], s28 offen nt
	buffer_load_dwordx4 v[74:77], v193, s[16:19], 0 offen offset:1024 nt
	v_lshlrev_b32_e32 v42, 2, v0
	v_bfe_u32 v43, v0, 2, 2
	v_and_or_b32 v98, v42, 12, v43
	v_and_or_b32 v6, v98, 7, v8
	v_ashrrev_i32_e32 v7, 31, v6
	s_movk_i32 s0, 0x160
	v_lshl_add_u64 v[6:7], v[6:7], 2, s[10:11]
	v_lshrrev_b32_e32 v121, 5, v0
	v_cmp_gt_u32_e64 s[0:1], s0, v0
	global_load_dword v125, v[6:7], off
	global_load_dword v126, v[6:7], off offset:64
	global_load_dword v127, v[6:7], off offset:96
	global_load_dword v190, v[6:7], off offset:32
	v_cndmask_b32_e64 v42, 10, v121, s[0:1]
	v_lshlrev_b32_e32 v42, 2, v42
	s_lshl_b32 s3, s2, 5
	v_and_b32_e32 v122, 31, v0
	global_load_dword v118, v42, s[12:13]
	v_or_b32_e32 v42, s3, v122
	v_ashrrev_i32_e32 v43, 31, v42
	v_lshl_add_u64 v[42:43], v[42:43], 2, s[8:9]
	global_load_dword v119, v[42:43], off
	s_mov_b32 s3, 0
	v_mul_u32_u24_e32 v131, 0x2600, v1
	v_cmp_gt_u32_e64 s[4:5], 16, v120
	s_and_saveexec_b64 s[6:7], s[4:5]
	s_movk_i32 s8, 0x260
	v_mov_b32_e32 v102, 0
	v_mad_u32_u24 v101, v120, s8, v131
	v_mov_b32_e32 v103, v102
	ds_write_b64 v101, v[102:103] offset:20056
	s_or_b64 exec, exec, s[6:7]
	v_cmp_lt_u32_e32 vcc, 10, v123
	s_waitcnt vmcnt(19)
	v_mul_f32_e32 v101, v87, v87
	v_mov_b32_e32 v106, v92
	s_waitcnt vmcnt(16)
	v_cndmask_b32_e64 v103, v97, 0, vcc
	v_cndmask_b32_e64 v102, v96, 0, vcc
	v_mov_b32_e32 v96, v91
	v_mov_b32_e32 v97, v83
	v_cndmask_b32_e64 v105, v95, 0, vcc
	v_cndmask_b32_e64 v104, v94, 0, vcc
	v_mov_b32_e32 v94, v90
	v_mov_b32_e32 v95, v82
	v_pk_mul_f32 v[96:97], v[96:97], v[96:97]
	v_mov_b32_e32 v107, v84
	v_fmac_f32_e32 v101, v86, v86
	v_pk_fma_f32 v[94:95], v[94:95], v[94:95], v[96:97]
	v_mov_b32_e32 v108, v93
	v_mov_b32_e32 v109, v85
	v_fmac_f32_e32 v101, v88, v88
	v_pk_fma_f32 v[94:95], v[106:107], v[106:107], v[94:95]
	v_fmac_f32_e32 v101, v89, v89
	v_pk_fma_f32 v[94:95], v[108:109], v[108:109], v[94:95]
	v_mov_b32_e32 v96, v79
	v_add_f32_e32 v94, v94, v101
	v_mov_b32_e32 v97, v105
	v_add_f32_e32 v101, v94, v95
	v_mov_b32_e32 v94, v78
	v_mov_b32_e32 v95, v104
	v_pk_mul_f32 v[96:97], v[96:97], v[96:97]
	s_mov_b32 s21, 0xf800000
	v_pk_fma_f32 v[94:95], v[94:95], v[94:95], v[96:97]
	v_mov_b32_e32 v96, v80
	v_mov_b32_e32 v97, v102
	v_pk_fma_f32 v[94:95], v[96:97], v[96:97], v[94:95]
	v_mov_b32_e32 v96, v81
	v_mov_b32_e32 v97, v103
	v_pk_fma_f32 v[94:95], v[96:97], v[96:97], v[94:95]
	v_mov_b32_e32 v135, 0x260
	v_add_f32_e32 v94, v101, v94
	v_add_f32_e32 v94, v94, v95
	v_mbcnt_lo_u32_b32 v95, -1, 0
	v_mbcnt_hi_u32_b32 v95, -1, v95
	v_and_b32_e32 v97, 64, v95
	v_xor_b32_e32 v96, 1, v95
	v_add_u32_e32 v101, 64, v97
	v_cmp_lt_i32_e32 vcc, v96, v101
	s_movk_i32 s8, 0x260
	v_add_u32_e32 v137, 0x4b00, v99
	v_cndmask_b32_e32 v96, v95, v96, vcc
	v_lshlrev_b32_e32 v97, 2, v96
	ds_bpermute_b32 v96, v97, v94
	s_movk_i32 s10, 0x1b5
	v_mov_b32_e32 v99, 0x36a00
	v_mov_b32_e32 v111, 0x666c0
	v_mov_b32_e32 v113, 0x6d400
	s_waitcnt lgkmcnt(0)
	v_add_f32_e32 v94, v94, v96
	v_xor_b32_e32 v96, 2, v95
	v_cmp_lt_i32_e32 vcc, v96, v101
	v_mov_b32_e32 v115, 0x74140
	s_mov_b32 s20, 0xbeb17218
	v_cndmask_b32_e32 v96, v95, v96, vcc
	v_lshlrev_b32_e32 v128, 2, v96
	ds_bpermute_b32 v96, v128, v94
	s_mov_b32 s22, 0x44132d1f
	v_mov_b32_e32 v161, 0xc47a0000
	s_waitcnt lgkmcnt(0)
	v_add_f32_e32 v94, v94, v96
	v_xor_b32_e32 v96, 4, v95
	v_cmp_lt_i32_e32 vcc, v96, v101
	s_nop 1
	v_cndmask_b32_e32 v96, v95, v96, vcc
	v_lshlrev_b32_e32 v129, 2, v96
	ds_bpermute_b32 v96, v129, v94
	s_waitcnt lgkmcnt(0)
	v_add_f32_e32 v94, v94, v96
	v_xor_b32_e32 v96, 8, v95
	v_cmp_lt_i32_e32 vcc, v96, v101
	s_nop 1
	v_cndmask_b32_e32 v96, v95, v96, vcc
	v_lshlrev_b32_e32 v130, 2, v96
	ds_bpermute_b32 v96, v130, v94
	s_waitcnt lgkmcnt(0)
	v_add_f32_e32 v94, v94, v96
	v_mul_f32_e32 v96, 0x4f800000, v94
	v_cmp_gt_f32_e32 vcc, s21, v94
	s_nop 1
	v_cndmask_b32_e32 v94, v94, v96, vcc
	v_sqrt_f32_e32 v96, v94
	s_nop 0
	v_add_u32_e32 v106, -1, v96
	v_fma_f32 v107, -v106, v96, v94
	v_cmp_ge_f32_e64 s[6:7], 0, v107
	v_add_u32_e32 v107, 1, v96
	s_nop 0
	v_cndmask_b32_e64 v106, v96, v106, s[6:7]
	v_fma_f32 v96, -v107, v96, v94
	v_cmp_lt_f32_e64 s[6:7], 0, v96
	s_nop 1
	v_cndmask_b32_e64 v96, v106, v107, s[6:7]
	v_mul_f32_e32 v106, 0x37800000, v96
	v_cndmask_b32_e32 v96, v96, v106, vcc
	v_cmp_class_f32_e32 vcc, v94, v135
	s_nop 1
	v_cndmask_b32_e32 v94, v96, v94, vcc
	v_add_f32_e32 v96, 0x29e12e13, v94
	v_div_scale_f32 v106, s[6:7], v96, v96, 1.0
	v_rcp_f32_e32 v107, v106
	v_mov_b32_e32 v94, 0
	v_cmp_gt_u32_e64 s[6:7], 48, v120
	v_mov_b32_e32 v116, v94
	v_fma_f32 v108, -v106, v107, 1.0
	v_fmac_f32_e32 v107, v108, v107
	v_div_scale_f32 v108, vcc, 1.0, v96, 1.0
	v_mul_f32_e32 v109, v108, v107
	v_fma_f32 v110, -v106, v109, v108
	v_fmac_f32_e32 v109, v110, v107
	v_fma_f32 v106, -v106, v109, v108
	v_div_fmas_f32 v106, v106, v107, v109
	v_div_fixup_f32 v96, v106, v96, 1.0
	v_lshlrev_b32_e32 v106, 3, v123
	v_pk_mul_f32 v[82:83], v[96:97], v[82:83] op_sel_hi:[0,1]
	v_pk_mul_f32 v[84:85], v[96:97], v[84:85] op_sel_hi:[0,1]
	v_pk_mul_f32 v[78:79], v[96:97], v[78:79] op_sel_hi:[0,1]
	v_pk_mul_f32 v[80:81], v[96:97], v[80:81] op_sel_hi:[0,1]
	v_mad_u32_u24 v100, v100, s8, v106
	v_cvt_pk_f16_f32 v82, v82, v83
	v_cvt_pk_f16_f32 v83, v84, v85
	v_cvt_pk_f16_f32 v78, v78, v79
	v_cvt_pk_f16_f32 v79, v80, v81
	ds_write2_b64 v100, v[82:83], v[78:79] offset0:32 offset1:48
	v_min_u32_e32 v82, 23, v120
	v_mov_b32_e32 v83, 0x2400
	v_lshl_or_b32 v138, v82, 4, v83
	v_xor_b32_e32 v83, 16, v95
	v_cmp_lt_i32_e32 vcc, v83, v101
	v_pk_mul_f32 v[90:91], v[96:97], v[90:91] op_sel_hi:[0,1]
	v_pk_mul_f32 v[92:93], v[96:97], v[92:93] op_sel_hi:[0,1]
	v_cndmask_b32_e32 v83, v95, v83, vcc
	v_lshlrev_b32_e32 v133, 2, v83
	v_xor_b32_e32 v83, 32, v95
	v_pk_mul_f32 v[86:87], v[96:97], v[86:87] op_sel_hi:[0,1]
	v_pk_mul_f32 v[88:89], v[96:97], v[88:89] op_sel_hi:[0,1]
	v_pk_mul_f32 v[78:79], v[96:97], v[104:105] op_sel_hi:[0,1]
	v_pk_mul_f32 v[80:81], v[96:97], v[102:103] op_sel_hi:[0,1]
	v_cmp_lt_i32_e32 vcc, v83, v101
	v_cvt_pk_f16_f32 v90, v90, v91
	v_cvt_pk_f16_f32 v91, v92, v93
	v_cvt_pk_f16_f32 v86, v86, v87
	v_cvt_pk_f16_f32 v87, v88, v89
	v_cvt_pk_f16_f32 v78, v78, v79
	v_cvt_pk_f16_f32 v79, v80, v81
	v_mov_b32_e32 v81, 0x17c00
	v_cndmask_b32_e32 v83, v95, v83, vcc
	ds_write2_b64 v100, v[90:91], v[86:87] offset1:16
	v_sub_u32_e64 v80, v123, 11 clamp
	v_lshl_or_b32 v81, v1, 7, v81
	v_lshlrev_b32_e32 v134, 2, v83
	v_or_b32_e32 v83, 64, v120
	v_mov_b32_e32 v86, 0x6d40
	v_mov_b32_e32 v87, 0xda80
	v_mov_b32_e32 v89, 0x147c0
	v_mov_b32_e32 v91, 0x1b500
	v_mov_b32_e32 v93, 0x28f80
	v_mov_b32_e32 v96, 0x2fcc0
	v_mov_b32_e32 v101, 0x3d740
	v_mov_b32_e32 v103, 0x44480
	v_mov_b32_e32 v105, 0x4b1c0
	v_mov_b32_e32 v107, 0x58c40
	v_or_b32_e32 v109, 0x3c0, v0
	v_mad_i32_i24 v80, v80, -8, v100
	v_lshrrev_b32_e32 v82, 1, v120
	v_lshl_add_u32 v139, v120, 2, v81
	v_and_or_b32 v140, v120, 48, v81
	v_lshlrev_b32_e32 v81, 3, v120
	v_mul_u32_u24_e32 v84, 0x1b5, v83
	v_lshl_add_u32 v85, v83, 3, v131
	v_mad_u32_u24 v86, v83, s10, v86
	v_mad_u32_u24 v87, v83, s10, v87
	v_mad_u32_u24 v89, v83, s10, v89
	v_mad_u32_u24 v91, v83, s10, v91
	v_mad_u32_u24 v93, v83, s10, v93
	v_mad_u32_u24 v96, v83, s10, v96
	v_mad_u32_u24 v99, v83, s10, v99
	v_mad_u32_u24 v101, v83, s10, v101
	v_mad_u32_u24 v103, v83, s10, v103
	v_mad_u32_u24 v105, v83, s10, v105
	v_mad_u32_u24 v107, v83, s10, v107
	v_mul_u32_u24_e32 v110, 0x1b5, v109
	v_mad_u32_u24 v111, v83, s10, v111
	v_mad_u32_u24 v113, v83, s10, v113
	v_mad_u32_u24 v83, v83, s10, v115
	ds_write_b64 v80, v[78:79] offset:512
	v_mul_u32_u24_e32 v78, 0x260, v123
	v_and_b32_e32 v82, 24, v82
	v_lshrrev_b32_e32 v84, 12, v84
	v_add_u32_e32 v141, v131, v81
	v_lshrrev_b32_e32 v86, 12, v86
	v_lshrrev_b32_e32 v87, 12, v87
	v_lshrrev_b32_e32 v89, 12, v89
	v_lshrrev_b32_e32 v91, 12, v91
	v_lshrrev_b32_e32 v93, 12, v93
	v_lshrrev_b32_e32 v96, 12, v96
	v_lshrrev_b32_e32 v99, 12, v99
	v_lshrrev_b32_e32 v101, 12, v101
	v_lshrrev_b32_e32 v103, 12, v103
	v_lshrrev_b32_e32 v105, 12, v105
	v_lshrrev_b32_e32 v107, 12, v107
	v_lshrrev_b32_e32 v110, 12, v110
	v_lshrrev_b32_e32 v111, 12, v111
	v_lshrrev_b32_e32 v113, 12, v113
	v_lshrrev_b32_e32 v83, 12, v83
	v_and_b32_e32 v79, 48, v0
	v_mad_u32_u24 v80, v98, s8, v131
	v_and_b32_e32 v84, 8, v84
	v_add_u32_e32 v81, 0x400, v141
	v_and_b32_e32 v86, 24, v86
	v_add_u32_e32 v88, 0x600, v141
	v_and_b32_e32 v87, 24, v87
	v_add_u32_e32 v90, 0x800, v141
	v_and_b32_e32 v89, 56, v89
	v_add_u32_e32 v92, 0xa00, v141
	v_and_b32_e32 v91, 56, v91
	v_add_u32_e32 v95, 0xe00, v141
	v_and_b32_e32 v93, 56, v93
	v_add_u32_e32 v98, 0x1000, v141
	v_and_b32_e32 v96, 56, v96
	v_add_u32_e32 v100, 0x1200, v141
	v_and_b32_e32 v99, 0x78, v99
	v_add_u32_e32 v102, 0x1400, v141
	v_and_b32_e32 v101, 0x78, v101
	v_add_u32_e32 v104, 0x1600, v141
	v_and_b32_e32 v103, 0x58, v103
	v_add_u32_e32 v106, 0x1800, v141
	v_and_b32_e32 v105, 0x58, v105
	v_add_u32_e32 v108, 0x1c00, v141
	v_and_b32_e32 v107, 0x78, v107
	v_lshl_add_u32 v109, v109, 3, v131
	v_and_b32_e32 v110, 0x78, v110
	v_add_u32_e32 v112, 0x2000, v141
	v_and_b32_e32 v111, 0x78, v111
	v_add_u32_e32 v114, 0x2200, v141
	v_and_b32_e32 v113, 0x78, v113
	v_add_u32_e32 v115, 0x2400, v141
	v_and_b32_e32 v83, 0xf8, v83
	s_movk_i32 s10, 0x4c00
	v_add_u32_e32 v78, v78, v82
	v_mad_u32_u24 v136, v123, s8, v79
	v_cmp_gt_u32_e64 s[8:9], 24, v120
	v_add3_u32 v142, v80, v79, s10
	v_add_u32_e32 v143, v85, v84
	v_add_u32_e32 v144, v81, v86
	v_add_u32_e32 v145, v88, v87
	v_add_u32_e32 v146, v90, v89
	v_add_u32_e32 v147, v92, v91
	v_add_u32_e32 v148, v95, v93
	v_add_u32_e32 v149, v98, v96
	v_add_u32_e32 v150, v100, v99
	v_add_u32_e32 v151, v102, v101
	v_add_u32_e32 v152, v104, v103
	v_add_u32_e32 v153, v106, v105
	v_add_u32_e32 v154, v108, v107
	v_add_u32_e32 v155, v109, v110
	v_add_u32_e32 v156, v112, v111
	v_add_u32_e32 v157, v114, v113
	v_add_u32_e32 v158, v115, v83
	v_add_u32_e32 v159, v80, v82
	v_add_u32_e32 v160, 64, v78
	v_mov_b32_e32 v96, 0xc604b4df
	v_mov_b32_e32 v95, v94
	v_mov_b32_e32 v98, v94
	v_mov_b32_e32 v99, v94
	v_mov_b32_e32 v100, v94
	v_mov_b32_e32 v101, v94
	v_mov_b32_e32 v102, v94
	v_mov_b32_e32 v103, v94
	v_mov_b32_e32 v104, v94
	v_mov_b32_e32 v105, v94
	v_mov_b32_e32 v106, v94
	v_mov_b32_e32 v107, v94
	v_mov_b32_e32 v108, v94
	v_mov_b32_e32 v109, v94
	v_mov_b32_e32 v110, v94
	v_mov_b32_e32 v111, v94
	v_mov_b32_e32 v112, v94
	v_mov_b32_e32 v113, v94
	v_mov_b32_e32 v114, v94
	v_mov_b32_e32 v115, v94
	v_mov_b32_e32 v117, v94
	s_waitcnt lgkmcnt(0)
	s_barrier
	s_mov_b32 s26, 0x2580
	s_mov_b32 s27, 0x3580
	s_mov_b32 s28, 0x4580
	buffer_load_dwordx4 v[6:9], v192, s[16:19], s26 offen nt
	buffer_load_dwordx4 v[10:13], v192, s[16:19], s26 offen offset:1024 nt
	buffer_load_dwordx4 v[18:21], v192, s[16:19], s26 offen offset:2048 nt
	buffer_load_dwordx4 v[22:25], v192, s[16:19], s26 offen offset:3072 nt
	buffer_load_dwordx4 v[26:29], v192, s[16:19], s27 offen nt
	buffer_load_dwordx4 v[30:33], v192, s[16:19], s27 offen offset:1024 nt
	buffer_load_dwordx4 v[38:41], v192, s[16:19], s27 offen offset:2048 nt
	buffer_load_dwordx4 v[42:45], v192, s[16:19], s27 offen offset:3072 nt
	buffer_load_dwordx4 v[50:53], v192, s[16:19], s28 offen nt
	buffer_load_dwordx4 v[186:189], v193, s[16:19], s26 offen offset:1024 nt
	s_waitcnt vmcnt(25)
	v_cvt_pk_f16_f32 v79, v4, v5
	v_cvt_pk_f16_f32 v78, v2, v3
	ds_write_b64 v141, v[78:79] offset:19456
	s_waitcnt vmcnt(24)
	v_cvt_pk_f16_f32 v79, v16, v17
	v_cvt_pk_f16_f32 v78, v14, v15
	ds_write_b64 v143, v[78:79] offset:19456
	s_waitcnt vmcnt(23)
	v_cvt_pk_f16_f32 v79, v36, v37
	v_cvt_pk_f16_f32 v78, v34, v35
	ds_write_b64 v144, v[78:79] offset:19456
	s_waitcnt vmcnt(22)
	v_cvt_pk_f16_f32 v79, v48, v49
	v_cvt_pk_f16_f32 v78, v46, v47
	ds_write_b64 v145, v[78:79] offset:19456
	s_waitcnt vmcnt(21)
	v_cvt_pk_f16_f32 v79, v56, v57
	v_cvt_pk_f16_f32 v78, v54, v55
	ds_write_b64 v146, v[78:79] offset:19456
	s_waitcnt vmcnt(20)
	v_cvt_pk_f16_f32 v79, v60, v61
	v_cvt_pk_f16_f32 v78, v58, v59
	ds_write_b64 v147, v[78:79] offset:19456
	s_waitcnt vmcnt(19)
	v_cvt_pk_f16_f32 v79, v64, v65
	v_cvt_pk_f16_f32 v78, v62, v63
	ds_write_b64 v141, v[78:79] offset:22568
	s_waitcnt vmcnt(18)
	v_cvt_pk_f16_f32 v79, v68, v69
	v_cvt_pk_f16_f32 v78, v66, v67
	ds_write_b64 v148, v[78:79] offset:19456
	s_waitcnt vmcnt(17)
	v_cvt_pk_f16_f32 v79, v72, v73
	v_cvt_pk_f16_f32 v78, v70, v71
	ds_write_b64 v149, v[78:79] offset:19456
	s_waitcnt vmcnt(16)
	v_cvt_pk_f16_f32 v79, v76, v77
	v_cvt_pk_f16_f32 v78, v74, v75
	s_and_saveexec_b64 s[12:13], s[8:9]
	ds_write_b64 v150, v[78:79] offset:19456
	s_or_b64 exec, exec, s[12:13]
	s_waitcnt vmcnt(10)
	v_cmp_lt_i32_e64 s[30:31], 1, v125
	v_cmp_lt_i32_e64 s[32:33], 1, v190
	v_cmp_lt_i32_e64 s[34:35], 1, v126
	v_cmp_lt_i32_e64 s[36:37], 1, v127
	v_cndmask_b32_e64 v191, 0, 1, s[30:31]
	v_cndmask_b32_e64 v190, 0, 2, s[32:33]
	v_cndmask_b32_e64 v126, 0, 4, s[34:35]
	v_cndmask_b32_e64 v127, 0, 8, s[36:37]
	v_or3_b32 v191, v191, v190, v126
	v_or_b32_e32 v191, v191, v127
	s_mov_b32 s26, 0x4b00
	s_mov_b32 s27, 0x5b00
	s_mov_b32 s28, 0x6b00
	buffer_load_dwordx4 v[2:5], v192, s[16:19], s26 offen nt
	buffer_load_dwordx4 v[14:17], v192, s[16:19], s26 offen offset:1024 nt
	buffer_load_dwordx4 v[34:37], v192, s[16:19], s26 offen offset:2048 nt
	buffer_load_dwordx4 v[46:49], v192, s[16:19], s26 offen offset:3072 nt
	buffer_load_dwordx4 v[54:57], v192, s[16:19], s27 offen nt
	buffer_load_dwordx4 v[58:61], v192, s[16:19], s27 offen offset:1024 nt
	buffer_load_dwordx4 v[62:65], v192, s[16:19], s27 offen offset:2048 nt
	buffer_load_dwordx4 v[66:69], v192, s[16:19], s27 offen offset:3072 nt
	buffer_load_dwordx4 v[70:73], v192, s[16:19], s28 offen nt
	buffer_load_dwordx4 v[74:77], v193, s[16:19], s26 offen offset:1024 nt
	s_mov_b32 s3, 0
	s_branch .LBB0_7

.LBB0_20:
	v_lshlrev_b32_e32 v2, 2, v123
	v_lshl_add_u32 v3, v120, 2, v131
	ds_write2st64_b32 v3, v94, v95 offset0:76 offset1:77
	ds_write2st64_b32 v3, v98, v99 offset0:78 offset1:79
	ds_write2st64_b32 v3, v100, v101 offset0:80 offset1:81
	ds_write2st64_b32 v3, v102, v103 offset0:82 offset1:83
	ds_write2st64_b32 v3, v104, v105 offset0:84 offset1:85
	ds_write2st64_b32 v3, v106, v107 offset0:86 offset1:87
	ds_write2st64_b32 v3, v108, v109 offset0:88 offset1:89
	ds_write2st64_b32 v3, v110, v111 offset0:90 offset1:91
	ds_write2st64_b32 v3, v112, v113 offset0:92 offset1:93
	ds_write2st64_b32 v3, v114, v115 offset0:94 offset1:95
	ds_write2st64_b32 v3, v116, v117 offset0:96 offset1:97
	v_mov_b32_e32 v3, 0
	s_waitcnt lgkmcnt(0)
	s_barrier
	s_and_saveexec_b64 s[4:5], s[0:1]
	s_cbranch_execz .LBB0_22
	v_lshlrev_b32_e32 v8, 1, v121
	v_lshrrev_b32_e32 v3, 4, v122
	v_or_b32_e32 v3, v8, v3
	v_lshl_or_b32 v9, v3, 8, v2
	v_add_u32_e32 v4, 0x4c00, v9
	v_add_u32_e32 v5, 0x7200, v9
	v_add_u32_e32 v6, 0x9800, v9
	v_add_u32_e32 v7, 0xbe00, v9
	ds_read2_b32 v[10:11], v4 offset1:16
	ds_read2_b32 v[12:13], v4 offset0:32 offset1:48
	ds_read2_b32 v[14:15], v5 offset1:16
	ds_read2_b32 v[16:17], v5 offset0:32 offset1:48
	ds_read2_b32 v[18:19], v6 offset1:16
	ds_read2_b32 v[20:21], v6 offset0:32 offset1:48
	ds_read2_b32 v[22:23], v7 offset1:16
	ds_read2_b32 v[24:25], v7 offset0:32 offset1:48
	v_add_u32_e32 v4, 0xe400, v9
	v_add_u32_e32 v5, 0x10a00, v9
	v_add_u32_e32 v6, 0x13000, v9
	v_add_u32_e32 v7, 0x15600, v9
	ds_read2_b32 v[26:27], v4 offset1:16
	ds_read2_b32 v[28:29], v4 offset0:32 offset1:48
	ds_read2_b32 v[30:31], v5 offset1:16
	ds_read2_b32 v[32:33], v5 offset0:32 offset1:48
	ds_read2_b32 v[34:35], v6 offset1:16
	ds_read2_b32 v[36:37], v6 offset0:32 offset1:48
	ds_read2_b32 v[38:39], v7 offset1:16
	v_sub_u32_e32 v4, 11, v8
	v_cvt_f32_i32_e32 v4, v4
	v_cmp_lt_u32_e32 vcc, 31, v0
	v_mul_f32_e32 v3, 0xbf38aa3b, v4
	v_mul_f32_e32 v3, v3, v4
	v_exp_f32_e32 v3, v3
	s_nop 0
	v_cndmask_b32_e32 v46, 1.0, v3, vcc
	s_waitcnt lgkmcnt(7)
	ds_read2_b32 v[40:41], v7 offset0:32 offset1:48
	v_add_f32_e32 v10, v10, v11
	v_add_f32_e32 v12, v12, v13
	v_add_f32_e32 v14, v14, v15
	v_add_f32_e32 v16, v16, v17
	v_add_f32_e32 v18, v18, v19
	v_add_f32_e32 v20, v20, v21
	v_add_f32_e32 v22, v22, v23
	v_add_f32_e32 v24, v24, v25
	v_add_f32_e32 v10, v10, v12
	v_add_f32_e32 v14, v14, v16
	v_add_f32_e32 v18, v18, v20
	v_add_f32_e32 v22, v22, v24
	v_add_f32_e32 v10, v10, v14
	v_add_f32_e32 v18, v18, v22
	v_add_f32_e32 v10, v10, v18
	s_waitcnt lgkmcnt(0)
	v_add_f32_e32 v26, v26, v27
	v_add_f32_e32 v28, v28, v29
	v_add_f32_e32 v30, v30, v31
	v_add_f32_e32 v32, v32, v33
	v_add_f32_e32 v34, v34, v35
	v_add_f32_e32 v36, v36, v37
	v_add_f32_e32 v38, v38, v39
	v_add_f32_e32 v40, v40, v41
	v_add_f32_e32 v26, v26, v28
	v_add_f32_e32 v30, v30, v32
	v_add_f32_e32 v34, v34, v36
	v_add_f32_e32 v38, v38, v40
	v_add_f32_e32 v26, v26, v30
	v_add_f32_e32 v34, v34, v38
	v_add_f32_e32 v26, v26, v34
	v_add_f32_e32 v2, v10, v26
	v_mul_f32_e32 v2, v46, v2
	v_max_f32_e32 v2, 0x2edbe6ff, v2
	v_log_f32_e32 v2, v2
	v_cmp_lt_i32_e32 vcc, 1, v119
	v_mul_f32_e32 v2, v118, v2
	s_nop 0
	v_cndmask_b32_e32 v3, 0, v2, vcc
.LBB0_22:
	s_or_b64 exec, exec, s[4:5]
	v_cmp_eq_u32_e32 vcc, 0, v120
	s_nop 4
	v_add_f32_dpp v2, v3, v3 quad_perm:[1,0,3,2] row_mask:0xf bank_mask:0xf
	s_nop 1
	v_add_f32_dpp v3, v2, v2 quad_perm:[2,3,0,1] row_mask:0xf bank_mask:0xf
	s_nop 1
	v_add_f32_dpp v2, v3, v3 row_ror:4 row_mask:0xf bank_mask:0xf
	s_nop 1
	v_add_f32_dpp v3, v2, v2 row_ror:8 row_mask:0xf bank_mask:0xf
	s_nop 0
	v_mov_b32_e32 v2, v3
	s_nop 1
	v_permlane16_swap_b32_e32 v2, v3
	v_add_f32_e32 v3, v2, v3
	v_mov_b32_e32 v2, v3
	s_nop 1
	v_permlane32_swap_b32_e32 v2, v3
	v_add_f32_e32 v2, v2, v3
	s_and_saveexec_b64 s[0:1], vcc
	s_cbranch_execz .LBB0_24
	v_mov_b32_e32 v3, 0x18000
	v_lshl_or_b32 v1, v1, 2, v3
	ds_write_b32 v1, v2
